# v15
# baseline (speedup 1.0000x reference)
_Z12pool1_kernelPKfS0_S0_S0_S0_S0_S0_S0_S0_S0_PfS1_:
	s_load_dwordx4 s[12:15], s[0:1], 0x0
	s_load_dwordx2 s[36:37], s[0:1], 0x48
	s_load_dwordx2 s[38:39], s[0:1], 0x58
	s_cmp_eq_u32 s2, 0
	s_movk_i32 s3, 0x80
	s_cselect_b64 s[4:5], -1, 0
	v_cmp_gt_u32_e64 s[10:11], s3, v0
	s_and_b64 s[6:7], s[4:5], s[10:11]
	s_and_saveexec_b64 s[4:5], s[6:7]
	s_cbranch_execz .LBB0_2
	v_mov_b32_e32 v1, 0
	v_lshlrev_b64 v[2:3], 2, v[0:1]
	s_waitcnt lgkmcnt(0)
	v_lshl_add_u64 v[4:5], s[36:37], 0, v[2:3]
	global_load_dword v253, v[4:5], off
	v_lshl_add_u64 v[254:255], s[38:39], 0, v[2:3]

.LBB0_5:
	v_mad_legacy_u16 v2, v6, s8, v4
	v_lshlrev_b16_e32 v8, 15, v2
	v_lshrrev_b16_e32 v2, 1, v2
	v_cmp_lt_u32_e32 vcc, s24, v6
	v_or_b32_e32 v2, v2, v8
	s_or_b64 s[0:1], vcc, s[0:1]
	v_cmp_gt_u16_e32 vcc, s9, v2
	v_add_u32_e32 v7, 0x200, v6
	v_mov_b32_e32 v6, v7
	v_cndmask_b32_e32 v2, 0, v5, vcc
	ds_write_b64 v1, v[2:3]
	v_add_u32_e32 v1, 0x1000, v1
	s_andn2_b64 exec, exec, s[0:1]
	s_cbranch_execnz .LBB0_5
	s_or_b64 exec, exec, s[0:1]
	s_mov_b32 s34, 0
	v_cmp_eq_u32_e64 s[0:1], 0, v0
	s_and_saveexec_b64 s[8:9], s[0:1]
	v_mov_b32_e32 v1, 8
	v_mov_b32_e32 v2, 0x23420
	ds_write_b32 v2, v1
	s_or_b64 exec, exec, s[8:9]
	v_lshlrev_b32_e32 v1, 2, v131
	v_or_b32_e32 v2, 0x22200, v1
	v_or_b32_e32 v3, 0x22300, v1
	s_waitcnt lgkmcnt(0)
	s_barrier
	ds_read_b32 v2, v2
	ds_read_b32 v3, v3
	s_load_dword s4, s[4:5], 0x0
	v_and_b32_e32 v202, 15, v0
	s_lshl_b32 s30, s31, 4
	v_or_b32_e32 v132, s30, v202
	s_waitcnt lgkmcnt(0)
	v_add_f32_e32 v2, v2, v3
	v_mbcnt_lo_u32_b32 v3, -1, 0
	v_mbcnt_hi_u32_b32 v3, -1, v3
	v_and_b32_e32 v4, 64, v3
	v_add_u32_e32 v4, 64, v4
	v_xor_b32_e32 v5, 32, v3
	v_cmp_lt_i32_e32 vcc, v5, v4
	v_mov_b32_e32 v133, 0
	v_lshrrev_b32_e32 v209, 4, v131
	v_cndmask_b32_e32 v5, v3, v5, vcc
	v_lshlrev_b32_e32 v200, 2, v5
	ds_bpermute_b32 v5, v200, v2
	v_mov_b32_e32 v100, v133
	v_mov_b32_e32 v101, v133
	v_and_b32_e32 v203, 48, v0
	v_mov_b32_e32 v98, v133
	s_waitcnt lgkmcnt(0)
	v_add_f32_e32 v2, v2, v5
	v_xor_b32_e32 v5, 16, v3
	v_cmp_lt_i32_e32 vcc, v5, v4
	v_mov_b32_e32 v99, v133
	v_mov_b64_e32 v[104:105], v[100:101]
	v_cndmask_b32_e32 v5, v3, v5, vcc
	v_lshlrev_b32_e32 v201, 2, v5
	ds_bpermute_b32 v5, v201, v2
	v_mov_b64_e32 v[108:109], v[100:101]
	v_mov_b64_e32 v[112:113], v[100:101]
	v_mov_b64_e32 v[116:117], v[100:101]
	v_mov_b64_e32 v[120:121], v[100:101]
	s_waitcnt lgkmcnt(0)
	v_add_f32_e32 v2, v2, v5
	v_xor_b32_e32 v5, 8, v3
	v_cmp_lt_i32_e32 vcc, v5, v4
	v_mov_b64_e32 v[124:125], v[100:101]
	v_mov_b64_e32 v[128:129], v[100:101]
	v_cndmask_b32_e32 v5, v3, v5, vcc
	v_lshlrev_b32_e32 v205, 2, v5
	ds_bpermute_b32 v5, v205, v2
	v_cmp_eq_u32_e64 s[8:9], 0, v131
	v_mov_b32_e32 v218, 0xff800000
	v_mov_b32_e32 v213, 0x23420
	v_mov_b64_e32 v[102:103], v[98:99]
	s_waitcnt lgkmcnt(0)
	v_add_f32_e32 v2, v2, v5
	v_xor_b32_e32 v5, 4, v3
	v_cmp_lt_i32_e32 vcc, v5, v4
	v_mov_b64_e32 v[106:107], v[98:99]
	v_mov_b64_e32 v[110:111], v[98:99]
	v_cndmask_b32_e32 v5, v3, v5, vcc
	v_lshlrev_b32_e32 v206, 2, v5
	ds_bpermute_b32 v5, v206, v2
	v_mov_b64_e32 v[114:115], v[98:99]
	v_mov_b64_e32 v[118:119], v[98:99]
	v_mov_b64_e32 v[122:123], v[98:99]
	v_mov_b64_e32 v[126:127], v[98:99]
	s_waitcnt lgkmcnt(0)
	v_add_f32_e32 v2, v2, v5
	v_xor_b32_e32 v5, 2, v3
	v_cmp_lt_i32_e32 vcc, v5, v4
	v_mov_b32_e32 v219, 0
	s_mov_b32 s35, s31
	v_cndmask_b32_e32 v5, v3, v5, vcc
	v_lshlrev_b32_e32 v207, 2, v5
	ds_bpermute_b32 v5, v207, v2
	v_mov_b32_e32 v138, 0
	v_mov_b32_e32 v139, v133
	v_mov_b32_e32 v136, 0
	v_mov_b32_e32 v137, v133
	s_waitcnt lgkmcnt(0)
	v_add_f32_e32 v2, v2, v5
	v_xor_b32_e32 v5, 1, v3
	v_cmp_lt_i32_e32 vcc, v5, v4
	v_lshlrev_b32_e32 v4, 3, v131
	v_mov_b32_e32 v144, 0
	v_cndmask_b32_e32 v3, v3, v5, vcc
	v_lshlrev_b32_e32 v208, 2, v3
	ds_bpermute_b32 v3, v208, v2
	v_mov_b32_e32 v145, v133
	v_mov_b32_e32 v142, 0
	v_mov_b32_e32 v143, v133
	v_mov_b32_e32 v150, 0
	s_waitcnt lgkmcnt(0)
	v_add_f32_e32 v2, v2, v3
	v_add_f32_e32 v2, s4, v2
	s_mul_i32 s4, s31, 0x2200
	s_add_i32 s24, s4, 0x11000
	v_mul_f32_e32 v210, 0x3fb8aa3b, v2
	s_movk_i32 s4, 0x220
	v_mov_b32_e32 v2, s24
	v_mad_u32_u24 v5, v202, s4, v2
	v_lshlrev_b64 v[2:3], 9, v[132:133]
	v_lshl_add_u64 v[2:3], s[6:7], 0, v[2:3]
	v_lshlrev_b32_e32 v132, 5, v209
	v_add_u32_e32 v212, s24, v4
	v_mad_u32_u24 v211, v202, s4, v203
	v_lshl_add_u64 v[134:135], v[2:3], 0, v[132:133]
	v_cmp_eq_u32_e64 s[6:7], 15, v202
	v_cmp_eq_u32_e64 s[4:5], 15, v131
	v_add_u32_e32 v214, v5, v203
	v_add_u32_e32 v215, 0x800, v212
	v_add_u32_e32 v216, 0x1000, v212
	v_add_u32_e32 v217, 0x1800, v212
	v_mov_b32_e32 v151, v133
	v_mov_b32_e32 v140, 0
	v_mov_b32_e32 v141, v133
	v_mov_b32_e32 v148, 0
	v_mov_b32_e32 v149, v133
	v_mov_b32_e32 v146, 0
	v_mov_b32_e32 v147, v133
	v_mov_b32_e32 v178, 0
	v_mov_b32_e32 v179, v133
	v_mov_b32_e32 v168, 0
	v_mov_b32_e32 v169, v133
	v_mov_b32_e32 v154, 0
	v_mov_b32_e32 v155, v133
	v_mov_b32_e32 v152, 0
	v_mov_b32_e32 v153, v133
	v_mov_b32_e32 v182, 0
	v_mov_b32_e32 v183, v133
	v_mov_b32_e32 v180, 0
	v_mov_b32_e32 v181, v133
	v_mov_b32_e32 v158, 0
	v_mov_b32_e32 v159, v133
	v_mov_b32_e32 v156, 0
	v_mov_b32_e32 v157, v133
	v_mov_b32_e32 v186, 0
	v_mov_b32_e32 v187, v133
	v_mov_b32_e32 v184, 0
	v_mov_b32_e32 v185, v133
	v_mov_b32_e32 v162, 0
	v_mov_b32_e32 v163, v133
	v_mov_b32_e32 v160, 0
	v_mov_b32_e32 v161, v133
	v_mov_b32_e32 v190, 0
	v_mov_b32_e32 v191, v133
	v_mov_b32_e32 v188, 0
	v_mov_b32_e32 v189, v133
	v_mov_b32_e32 v166, 0
	v_mov_b32_e32 v167, v133
	v_mov_b32_e32 v164, 0
	v_mov_b32_e32 v165, v133
	v_mov_b32_e32 v194, 0
	v_mov_b32_e32 v195, v133
	v_mov_b32_e32 v192, 0
	v_mov_b32_e32 v193, v133
	v_mov_b32_e32 v172, 0
	v_mov_b32_e32 v173, v133
	v_mov_b32_e32 v170, 0
	v_mov_b32_e32 v171, v133
	v_mov_b32_e32 v198, 0
	v_mov_b32_e32 v199, v133
	v_mov_b32_e32 v196, 0
	v_mov_b32_e32 v197, v133
	v_mov_b32_e32 v176, 0
	v_mov_b32_e32 v177, v133
	v_mov_b32_e32 v174, 0
	v_mov_b32_e32 v175, v133
	s_cmp_eq_u32 s2, 0
	s_cselect_b64 s[24:25], -1, 0
	s_and_b64 s[24:25], s[24:25], s[10:11]
	s_and_saveexec_b64 s[26:27], s[24:25]
	s_cbranch_execz .Lp1_noinit
	global_store_dword v[254:255], v253, off
.Lp1_noinit:
	s_or_b64 exec, exec, s[26:27]
